# attention units mapped so that the 12 workgroups of an XCD walk consecutive units (K/V halo shared in that XCD's L2); conversion reload addressing by scalar base + 32-bit offsets
# baseline (speedup 1.0000x reference)
; #define LAS __attribute__((address_space(3)))
; DI unsigned pk4_fp8(float a, float b, float c, float d) { unsigned p = 0u; p = __builtin_amdgcn_cvt_pk_fp8_f32(f8clamp(a), f8clamp(b), p, false); p = __builtin_amdgcn_cvt_pk_fp8_f32(f8clamp(c), f8clamp(d), p, true); return p; }
; DI void f8_convert_reload(f32x4 (&v)[4][4], int hb, float sc, LAS unsigned char* scr, bool reload, const F8Tile& dn, int lane) {
;     const int nq = lane & 15, kq = lane >> 4;
; #pragma unroll
;     for (int it = 0; it < 4; ++it) {
; #pragma unroll
;         for (int i = 0; i < 4; ++i) *(LAS unsigned*)(scr + (4 * nq + i) * 132 + hb * 64 + it * 16 + kq * 4) = pk4_fp8(v[it][0][i] * sc, v[it][1][i] * sc, v[it][2][i] * sc, v[it][3][i] * sc);
;         if (reload) {
; #pragma unroll
;             for (int j = 0; j < 4; ++j) v[it][j] = __builtin_nontemporal_load((const f32x4*)(dn.W + (size_t)(dn.k0 + hb * 64 + it * 16 + kq * 4 + j) * dn.N + dn.n0 + 4 * nq)); } }
; }
.Lcvw1:
	s_waitcnt vmcnt(28)
	v_mul_f32_e32 v134, 0x42800000, v118
	v_mul_f32_e32 v191, 0x42800000, v114
	v_med3_f32 v134, v134, s25, v189
	v_med3_f32 v191, v191, s25, v189
	v_mov_b32_e32 v193, 0
	v_cvt_pk_fp8_f32 v193, v134, v191
	v_mul_f32_e32 v192, 0x42800000, v126
	v_mul_f32_e32 v134, 0x42800000, v122
	v_med3_f32 v191, v192, s25, v189
	v_med3_f32 v134, v134, s25, v189
	v_cvt_pk_fp8_f32 v193, v191, v134 op_sel:[0,0,1]
	v_mul_f32_e32 v134, 0x42800000, v119
	v_mul_f32_e32 v191, 0x42800000, v115
	v_med3_f32 v134, v134, s25, v189
	v_med3_f32 v191, v191, s25, v189
	v_mov_b32_e32 v194, 0
	v_cvt_pk_fp8_f32 v194, v134, v191
	v_mul_f32_e32 v192, 0x42800000, v127
	v_mul_f32_e32 v134, 0x42800000, v123
	v_med3_f32 v191, v192, s25, v189
	v_med3_f32 v134, v134, s25, v189
	v_cvt_pk_fp8_f32 v194, v191, v134 op_sel:[0,0,1]
	v_mul_f32_e32 v134, 0x42800000, v120
	v_mul_f32_e32 v191, 0x42800000, v116
	v_med3_f32 v134, v134, s25, v189
	v_med3_f32 v191, v191, s25, v189
	v_mov_b32_e32 v195, 0
	v_cvt_pk_fp8_f32 v195, v134, v191
	v_mul_f32_e32 v192, 0x42800000, v128
	v_mul_f32_e32 v134, 0x42800000, v124
	v_med3_f32 v191, v192, s25, v189
	v_med3_f32 v134, v134, s25, v189
	v_cvt_pk_fp8_f32 v195, v191, v134 op_sel:[0,0,1]
	v_mul_f32_e32 v134, 0x42800000, v121
	v_mul_f32_e32 v191, 0x42800000, v117
	v_med3_f32 v134, v134, s25, v189
	v_med3_f32 v191, v191, s25, v189
	v_mov_b32_e32 v196, 0
	v_cvt_pk_fp8_f32 v196, v134, v191
	v_mul_f32_e32 v192, 0x42800000, v129
	v_mul_f32_e32 v134, 0x42800000, v125
	v_med3_f32 v191, v192, s25, v189
	v_med3_f32 v134, v134, s25, v189
	v_cvt_pk_fp8_f32 v196, v191, v134 op_sel:[0,0,1]
	v_cndmask_b32_e64 v134, 0, 1, s[16:17]
	v_cmp_ne_u32_e64 s[2:3], 1, v134
	s_andn2_b64 vcc, exec, s[16:17]
	v_lshlrev_b32_e32 v134, 2, v132
	ds_write2_b32 v190, v193, v194 offset1:33
	ds_write2_b32 v190, v195, v196 offset0:66 offset1:99
	s_cbranch_vccnz .LBB0_154
	s_mul_i32 s30, s27, s18
	s_add_i32 s30, s30, s4
	s_lshl_b32 s30, s30, 2
	s_add_u32 s16, s8, s30
	s_addc_u32 s17, s9, 0
	s_lshl_b32 s31, s18, 2
	v_mad_u32_u24 v118, v1, s31, v134
	v_mad_u32_u24 v114, v133, s31, v134
	v_mad_u32_u24 v126, v158, s31, v134
	v_mad_u32_u24 v122, v159, s31, v134
	global_load_dwordx4 v[118:121], v118, s[16:17] nt
	global_load_dwordx4 v[114:117], v114, s[16:17] nt
	global_load_dwordx4 v[126:129], v126, s[16:17] nt
	global_load_dwordx4 v[122:125], v122, s[16:17] nt
.LBB0_154:
	s_waitcnt vmcnt(28)
	v_mul_f32_e32 v191, 0x42800000, v102
	v_mul_f32_e32 v192, 0x42800000, v98
	v_med3_f32 v191, v191, s25, v189
	v_med3_f32 v192, v192, s25, v189
	v_mov_b32_e32 v194, 0
	v_cvt_pk_fp8_f32 v194, v191, v192
	v_mul_f32_e32 v193, 0x42800000, v110
	v_mul_f32_e32 v191, 0x42800000, v106
	v_med3_f32 v192, v193, s25, v189
	v_med3_f32 v191, v191, s25, v189
	v_cvt_pk_fp8_f32 v194, v192, v191 op_sel:[0,0,1]
	v_mul_f32_e32 v191, 0x42800000, v103
	v_mul_f32_e32 v192, 0x42800000, v99
	v_med3_f32 v191, v191, s25, v189
	v_med3_f32 v192, v192, s25, v189
	v_mov_b32_e32 v195, 0
	v_cvt_pk_fp8_f32 v195, v191, v192
	v_mul_f32_e32 v193, 0x42800000, v111
	v_mul_f32_e32 v191, 0x42800000, v107
	v_med3_f32 v192, v193, s25, v189
	v_med3_f32 v191, v191, s25, v189
	v_cvt_pk_fp8_f32 v195, v192, v191 op_sel:[0,0,1]
	v_mul_f32_e32 v191, 0x42800000, v104
	v_mul_f32_e32 v192, 0x42800000, v100
	v_med3_f32 v191, v191, s25, v189
	v_med3_f32 v192, v192, s25, v189
	v_mov_b32_e32 v196, 0
	v_cvt_pk_fp8_f32 v196, v191, v192
	v_mul_f32_e32 v193, 0x42800000, v112
	v_mul_f32_e32 v191, 0x42800000, v108
	v_med3_f32 v192, v193, s25, v189
	v_med3_f32 v191, v191, s25, v189
	v_cvt_pk_fp8_f32 v196, v192, v191 op_sel:[0,0,1]
	v_mul_f32_e32 v191, 0x42800000, v105
	v_mul_f32_e32 v192, 0x42800000, v101
	v_med3_f32 v191, v191, s25, v189
	v_med3_f32 v192, v192, s25, v189
	v_mov_b32_e32 v197, 0
	v_cvt_pk_fp8_f32 v197, v191, v192
	v_mul_f32_e32 v193, 0x42800000, v113
	v_mul_f32_e32 v191, 0x42800000, v109
	v_med3_f32 v192, v193, s25, v189
	v_med3_f32 v191, v191, s25, v189
	v_cvt_pk_fp8_f32 v197, v192, v191 op_sel:[0,0,1]
	s_and_b64 vcc, exec, s[2:3]
	ds_write2_b32 v190, v194, v195 offset0:4 offset1:37
	ds_write2_b32 v190, v196, v197 offset0:70 offset1:103
	s_cbranch_vccnz .LBB0_156
	s_mul_i32 s30, s27, s18
	s_add_i32 s30, s30, s4
	s_lshl_b32 s30, s30, 2
	s_add_u32 s16, s8, s30
	s_addc_u32 s17, s9, 0
	s_lshl_b32 s31, s18, 2
	v_mad_u32_u24 v102, v160, s31, v134
	v_mad_u32_u24 v98, v161, s31, v134
	v_mad_u32_u24 v110, v162, s31, v134
	v_mad_u32_u24 v106, v163, s31, v134
	global_load_dwordx4 v[102:105], v102, s[16:17] nt
	global_load_dwordx4 v[98:101], v98, s[16:17] nt
	global_load_dwordx4 v[110:113], v110, s[16:17] nt
	global_load_dwordx4 v[106:109], v106, s[16:17] nt
; #define LAS __attribute__((address_space(3)))
; DI unsigned pk4_fp8(float a, float b, float c, float d) { unsigned p = 0u; p = __builtin_amdgcn_cvt_pk_fp8_f32(f8clamp(a), f8clamp(b), p, false); p = __builtin_amdgcn_cvt_pk_fp8_f32(f8clamp(c), f8clamp(d), p, true); return p; }
; DI void f8_convert_reload(f32x4 (&v)[4][4], int hb, float sc, LAS unsigned char* scr, bool reload, const F8Tile& dn, int lane) {
;     const int nq = lane & 15, kq = lane >> 4;
; #pragma unroll
;     for (int it = 0; it < 4; ++it) {
; #pragma unroll
;         for (int i = 0; i < 4; ++i) *(LAS unsigned*)(scr + (4 * nq + i) * 132 + hb * 64 + it * 16 + kq * 4) = pk4_fp8(v[it][0][i] * sc, v[it][1][i] * sc, v[it][2][i] * sc, v[it][3][i] * sc);
;         if (reload) {
; #pragma unroll
;             for (int j = 0; j < 4; ++j) v[it][j] = __builtin_nontemporal_load((const f32x4*)(dn.W + (size_t)(dn.k0 + hb * 64 + it * 16 + kq * 4 + j) * dn.N + dn.n0 + 4 * nq)); } }
; }
.LBB0_156:
	s_waitcnt vmcnt(28)
	v_mul_f32_e32 v191, 0x42800000, v86
	v_mul_f32_e32 v192, 0x42800000, v82
	v_med3_f32 v191, v191, s25, v189
	v_med3_f32 v192, v192, s25, v189
	v_mov_b32_e32 v194, 0
	v_cvt_pk_fp8_f32 v194, v191, v192
	v_mul_f32_e32 v193, 0x42800000, v94
	v_mul_f32_e32 v191, 0x42800000, v90
	v_med3_f32 v192, v193, s25, v189
	v_med3_f32 v191, v191, s25, v189
	v_cvt_pk_fp8_f32 v194, v192, v191 op_sel:[0,0,1]
	v_mul_f32_e32 v191, 0x42800000, v87
	v_mul_f32_e32 v192, 0x42800000, v83
	v_med3_f32 v191, v191, s25, v189
	v_med3_f32 v192, v192, s25, v189
	v_mov_b32_e32 v195, 0
	v_cvt_pk_fp8_f32 v195, v191, v192
	v_mul_f32_e32 v193, 0x42800000, v95
	v_mul_f32_e32 v191, 0x42800000, v91
	v_med3_f32 v192, v193, s25, v189
	v_med3_f32 v191, v191, s25, v189
	v_cvt_pk_fp8_f32 v195, v192, v191 op_sel:[0,0,1]
	v_mul_f32_e32 v191, 0x42800000, v88
	v_mul_f32_e32 v192, 0x42800000, v84
	v_med3_f32 v191, v191, s25, v189
	v_med3_f32 v192, v192, s25, v189
	v_mov_b32_e32 v196, 0
	v_cvt_pk_fp8_f32 v196, v191, v192
	v_mul_f32_e32 v193, 0x42800000, v96
	v_mul_f32_e32 v191, 0x42800000, v92
	v_med3_f32 v192, v193, s25, v189
	v_med3_f32 v191, v191, s25, v189
	v_cvt_pk_fp8_f32 v196, v192, v191 op_sel:[0,0,1]
	v_mul_f32_e32 v191, 0x42800000, v89
	v_mul_f32_e32 v192, 0x42800000, v85
	v_med3_f32 v191, v191, s25, v189
	v_med3_f32 v192, v192, s25, v189
	v_mov_b32_e32 v197, 0
	v_cvt_pk_fp8_f32 v197, v191, v192
	v_mul_f32_e32 v193, 0x42800000, v97
	v_mul_f32_e32 v191, 0x42800000, v93
	v_med3_f32 v192, v193, s25, v189
	v_med3_f32 v191, v191, s25, v189
	v_cvt_pk_fp8_f32 v197, v192, v191 op_sel:[0,0,1]
	s_and_b64 vcc, exec, s[2:3]
	ds_write2_b32 v190, v194, v195 offset0:8 offset1:41
	ds_write2_b32 v190, v196, v197 offset0:74 offset1:107
	s_cbranch_vccnz .LBB0_158
	s_mul_i32 s30, s27, s18
	s_add_i32 s30, s30, s4
	s_lshl_b32 s30, s30, 2
	s_add_u32 s16, s8, s30
	s_addc_u32 s17, s9, 0
	s_lshl_b32 s31, s18, 2
	v_mad_u32_u24 v86, v164, s31, v134
	v_mad_u32_u24 v82, v165, s31, v134
	v_mad_u32_u24 v94, v166, s31, v134
	v_mad_u32_u24 v90, v167, s31, v134
	global_load_dwordx4 v[86:89], v86, s[16:17] nt
	global_load_dwordx4 v[82:85], v82, s[16:17] nt
	global_load_dwordx4 v[94:97], v94, s[16:17] nt
	global_load_dwordx4 v[90:93], v90, s[16:17] nt
.LBB0_158:
	s_waitcnt vmcnt(28)
	v_mul_f32_e32 v191, 0x42800000, v70
	v_mul_f32_e32 v192, 0x42800000, v66
	v_med3_f32 v191, v191, s25, v189
	v_med3_f32 v192, v192, s25, v189
	v_mov_b32_e32 v194, 0
	v_cvt_pk_fp8_f32 v194, v191, v192
	v_mul_f32_e32 v193, 0x42800000, v74
	v_mul_f32_e32 v191, 0x42800000, v78
	v_med3_f32 v192, v193, s25, v189
	v_med3_f32 v191, v191, s25, v189
	v_cvt_pk_fp8_f32 v194, v192, v191 op_sel:[0,0,1]
	v_mul_f32_e32 v191, 0x42800000, v71
	v_mul_f32_e32 v192, 0x42800000, v67
	v_med3_f32 v191, v191, s25, v189
	v_med3_f32 v192, v192, s25, v189
	v_mov_b32_e32 v195, 0
	v_cvt_pk_fp8_f32 v195, v191, v192
	v_mul_f32_e32 v193, 0x42800000, v75
	v_mul_f32_e32 v191, 0x42800000, v79
	v_med3_f32 v192, v193, s25, v189
	v_med3_f32 v191, v191, s25, v189
	v_cvt_pk_fp8_f32 v195, v192, v191 op_sel:[0,0,1]
	v_mul_f32_e32 v191, 0x42800000, v72
	v_mul_f32_e32 v192, 0x42800000, v68
	v_med3_f32 v191, v191, s25, v189
	v_med3_f32 v192, v192, s25, v189
	v_mov_b32_e32 v196, 0
	v_cvt_pk_fp8_f32 v196, v191, v192
	v_mul_f32_e32 v193, 0x42800000, v76
	v_mul_f32_e32 v191, 0x42800000, v80
	v_med3_f32 v192, v193, s25, v189
	v_med3_f32 v191, v191, s25, v189
	v_cvt_pk_fp8_f32 v196, v192, v191 op_sel:[0,0,1]
	v_mul_f32_e32 v191, 0x42800000, v73
	v_mul_f32_e32 v192, 0x42800000, v69
	v_med3_f32 v191, v191, s25, v189
	v_med3_f32 v192, v192, s25, v189
	v_mov_b32_e32 v197, 0
	v_cvt_pk_fp8_f32 v197, v191, v192
	v_mul_f32_e32 v193, 0x42800000, v77
	v_mul_f32_e32 v191, 0x42800000, v81
	v_med3_f32 v192, v193, s25, v189
	v_med3_f32 v191, v191, s25, v189
	v_cvt_pk_fp8_f32 v197, v192, v191 op_sel:[0,0,1]
	s_and_b64 vcc, exec, s[2:3]
	ds_write2_b32 v190, v194, v195 offset0:12 offset1:45
	ds_write2_b32 v190, v196, v197 offset0:78 offset1:111
	s_cbranch_vccnz .LBB0_160
	s_mul_i32 s30, s27, s18
	s_add_i32 s30, s30, s4
	s_lshl_b32 s30, s30, 2
	s_add_u32 s16, s8, s30
	s_addc_u32 s17, s9, 0
	s_lshl_b32 s31, s18, 2
	v_mad_u32_u24 v70, v168, s31, v134
	v_mad_u32_u24 v66, v169, s31, v134
	v_mad_u32_u24 v74, v170, s31, v134
	v_mad_u32_u24 v78, v171, s31, v134
	global_load_dwordx4 v[70:73], v70, s[16:17] nt
	global_load_dwordx4 v[66:69], v66, s[16:17] nt
	global_load_dwordx4 v[74:77], v74, s[16:17] nt
	global_load_dwordx4 v[78:81], v78, s[16:17] nt
.LBB0_160:
	s_waitcnt vmcnt(28)
	v_mul_f32_e32 v191, 0x42800000, v54
	v_mul_f32_e32 v192, 0x42800000, v50
	v_med3_f32 v191, v191, s25, v189
	v_med3_f32 v192, v192, s25, v189
	v_mov_b32_e32 v194, 0
	v_cvt_pk_fp8_f32 v194, v191, v192
	v_mul_f32_e32 v193, 0x42800000, v62
	v_mul_f32_e32 v191, 0x42800000, v58
	v_med3_f32 v192, v193, s25, v189
	v_med3_f32 v191, v191, s25, v189
	v_cvt_pk_fp8_f32 v194, v192, v191 op_sel:[0,0,1]
	v_mul_f32_e32 v191, 0x42800000, v55
	v_mul_f32_e32 v192, 0x42800000, v51
	v_med3_f32 v191, v191, s25, v189
	v_med3_f32 v192, v192, s25, v189
	v_mov_b32_e32 v195, 0
	v_cvt_pk_fp8_f32 v195, v191, v192
	v_mul_f32_e32 v193, 0x42800000, v63
	v_mul_f32_e32 v191, 0x42800000, v59
	v_med3_f32 v192, v193, s25, v189
	v_med3_f32 v191, v191, s25, v189
	v_cvt_pk_fp8_f32 v195, v192, v191 op_sel:[0,0,1]
	v_mul_f32_e32 v191, 0x42800000, v56
	v_mul_f32_e32 v192, 0x42800000, v52
	v_med3_f32 v191, v191, s25, v189
	v_med3_f32 v192, v192, s25, v189
	v_mov_b32_e32 v196, 0
	v_cvt_pk_fp8_f32 v196, v191, v192
	v_mul_f32_e32 v193, 0x42800000, v64
	v_mul_f32_e32 v191, 0x42800000, v60
	v_med3_f32 v192, v193, s25, v189
	v_med3_f32 v191, v191, s25, v189
	v_cvt_pk_fp8_f32 v196, v192, v191 op_sel:[0,0,1]
	v_mul_f32_e32 v191, 0x42800000, v57
	v_mul_f32_e32 v192, 0x42800000, v53
	v_med3_f32 v191, v191, s25, v189
	v_med3_f32 v192, v192, s25, v189
	v_mov_b32_e32 v197, 0
	v_cvt_pk_fp8_f32 v197, v191, v192
	v_mul_f32_e32 v193, 0x42800000, v65
	v_mul_f32_e32 v191, 0x42800000, v61
	v_med3_f32 v192, v193, s25, v189
	v_med3_f32 v191, v191, s25, v189
	v_cvt_pk_fp8_f32 v197, v192, v191 op_sel:[0,0,1]
	s_and_b64 vcc, exec, s[2:3]
	ds_write2_b32 v190, v194, v195 offset0:16 offset1:49
	ds_write2_b32 v190, v196, v197 offset0:82 offset1:115
	s_cbranch_vccnz .LBB0_162
	s_mul_i32 s30, s27, s18
	s_add_i32 s30, s30, s4
	s_lshl_b32 s30, s30, 2
	s_add_u32 s16, s8, s30
	s_addc_u32 s17, s9, 0
	s_lshl_b32 s31, s18, 2
	v_mad_u32_u24 v54, v172, s31, v134
	v_mad_u32_u24 v50, v173, s31, v134
	v_mad_u32_u24 v62, v174, s31, v134
	v_mad_u32_u24 v58, v175, s31, v134
	global_load_dwordx4 v[54:57], v54, s[16:17] nt
	global_load_dwordx4 v[50:53], v50, s[16:17] nt
	global_load_dwordx4 v[62:65], v62, s[16:17] nt
	global_load_dwordx4 v[58:61], v58, s[16:17] nt
; #define LAS __attribute__((address_space(3)))
; DI unsigned pk4_fp8(float a, float b, float c, float d) { unsigned p = 0u; p = __builtin_amdgcn_cvt_pk_fp8_f32(f8clamp(a), f8clamp(b), p, false); p = __builtin_amdgcn_cvt_pk_fp8_f32(f8clamp(c), f8clamp(d), p, true); return p; }
; DI void f8_convert_reload(f32x4 (&v)[4][4], int hb, float sc, LAS unsigned char* scr, bool reload, const F8Tile& dn, int lane) {
;     const int nq = lane & 15, kq = lane >> 4;
; #pragma unroll
;     for (int it = 0; it < 4; ++it) {
; #pragma unroll
;         for (int i = 0; i < 4; ++i) *(LAS unsigned*)(scr + (4 * nq + i) * 132 + hb * 64 + it * 16 + kq * 4) = pk4_fp8(v[it][0][i] * sc, v[it][1][i] * sc, v[it][2][i] * sc, v[it][3][i] * sc);
;         if (reload) {
; #pragma unroll
;             for (int j = 0; j < 4; ++j) v[it][j] = __builtin_nontemporal_load((const f32x4*)(dn.W + (size_t)(dn.k0 + hb * 64 + it * 16 + kq * 4 + j) * dn.N + dn.n0 + 4 * nq)); } }
; }
.LBB0_162:
	s_waitcnt vmcnt(28)
	v_mul_f32_e32 v191, 0x42800000, v38
	v_mul_f32_e32 v192, 0x42800000, v34
	v_med3_f32 v191, v191, s25, v189
	v_med3_f32 v192, v192, s25, v189
	v_mov_b32_e32 v194, 0
	v_cvt_pk_fp8_f32 v194, v191, v192
	v_mul_f32_e32 v193, 0x42800000, v46
	v_mul_f32_e32 v191, 0x42800000, v42
	v_med3_f32 v192, v193, s25, v189
	v_med3_f32 v191, v191, s25, v189
	v_cvt_pk_fp8_f32 v194, v192, v191 op_sel:[0,0,1]
	v_mul_f32_e32 v191, 0x42800000, v39
	v_mul_f32_e32 v192, 0x42800000, v35
	v_med3_f32 v191, v191, s25, v189
	v_med3_f32 v192, v192, s25, v189
	v_mov_b32_e32 v195, 0
	v_cvt_pk_fp8_f32 v195, v191, v192
	v_mul_f32_e32 v193, 0x42800000, v47
	v_mul_f32_e32 v191, 0x42800000, v43
	v_med3_f32 v192, v193, s25, v189
	v_med3_f32 v191, v191, s25, v189
	v_cvt_pk_fp8_f32 v195, v192, v191 op_sel:[0,0,1]
	v_mul_f32_e32 v191, 0x42800000, v40
	v_mul_f32_e32 v192, 0x42800000, v36
	v_med3_f32 v191, v191, s25, v189
	v_med3_f32 v192, v192, s25, v189
	v_mov_b32_e32 v196, 0
	v_cvt_pk_fp8_f32 v196, v191, v192
	v_mul_f32_e32 v193, 0x42800000, v48
	v_mul_f32_e32 v191, 0x42800000, v44
	v_med3_f32 v192, v193, s25, v189
	v_med3_f32 v191, v191, s25, v189
	v_cvt_pk_fp8_f32 v196, v192, v191 op_sel:[0,0,1]
	v_mul_f32_e32 v191, 0x42800000, v41
	v_mul_f32_e32 v192, 0x42800000, v37
	v_med3_f32 v191, v191, s25, v189
	v_med3_f32 v192, v192, s25, v189
	v_mov_b32_e32 v197, 0
	v_cvt_pk_fp8_f32 v197, v191, v192
	v_mul_f32_e32 v193, 0x42800000, v49
	v_mul_f32_e32 v191, 0x42800000, v45
	v_med3_f32 v192, v193, s25, v189
	v_med3_f32 v191, v191, s25, v189
	v_cvt_pk_fp8_f32 v197, v192, v191 op_sel:[0,0,1]
	s_and_b64 vcc, exec, s[2:3]
	ds_write2_b32 v190, v194, v195 offset0:20 offset1:53
	ds_write2_b32 v190, v196, v197 offset0:86 offset1:119
	s_cbranch_vccnz .LBB0_164
	s_mul_i32 s30, s27, s18
	s_add_i32 s30, s30, s4
	s_lshl_b32 s30, s30, 2
	s_add_u32 s16, s8, s30
	s_addc_u32 s17, s9, 0
	s_lshl_b32 s31, s18, 2
	v_mad_u32_u24 v38, v176, s31, v134
	v_mad_u32_u24 v34, v177, s31, v134
	v_mad_u32_u24 v46, v178, s31, v134
	v_mad_u32_u24 v42, v179, s31, v134
	global_load_dwordx4 v[38:41], v38, s[16:17] nt
	global_load_dwordx4 v[34:37], v34, s[16:17] nt
	global_load_dwordx4 v[46:49], v46, s[16:17] nt
	global_load_dwordx4 v[42:45], v42, s[16:17] nt
.LBB0_164:
	s_waitcnt vmcnt(28)
	v_mul_f32_e32 v191, 0x42800000, v22
	v_mul_f32_e32 v192, 0x42800000, v18
	v_med3_f32 v191, v191, s25, v189
	v_med3_f32 v192, v192, s25, v189
	v_mov_b32_e32 v194, 0
	v_cvt_pk_fp8_f32 v194, v191, v192
	v_mul_f32_e32 v193, 0x42800000, v30
	v_mul_f32_e32 v191, 0x42800000, v26
	v_med3_f32 v192, v193, s25, v189
	v_med3_f32 v191, v191, s25, v189
	v_cvt_pk_fp8_f32 v194, v192, v191 op_sel:[0,0,1]
	v_mul_f32_e32 v191, 0x42800000, v23
	v_mul_f32_e32 v192, 0x42800000, v19
	v_med3_f32 v191, v191, s25, v189
	v_med3_f32 v192, v192, s25, v189
	v_mov_b32_e32 v195, 0
	v_cvt_pk_fp8_f32 v195, v191, v192
	v_mul_f32_e32 v193, 0x42800000, v31
	v_mul_f32_e32 v191, 0x42800000, v27
	v_med3_f32 v192, v193, s25, v189
	v_med3_f32 v191, v191, s25, v189
	v_cvt_pk_fp8_f32 v195, v192, v191 op_sel:[0,0,1]
	v_mul_f32_e32 v191, 0x42800000, v24
	v_mul_f32_e32 v192, 0x42800000, v20
	v_med3_f32 v191, v191, s25, v189
	v_med3_f32 v192, v192, s25, v189
	v_mov_b32_e32 v196, 0
	v_cvt_pk_fp8_f32 v196, v191, v192
	v_mul_f32_e32 v193, 0x42800000, v32
	v_mul_f32_e32 v191, 0x42800000, v28
	v_med3_f32 v192, v193, s25, v189
	v_med3_f32 v191, v191, s25, v189
	v_cvt_pk_fp8_f32 v196, v192, v191 op_sel:[0,0,1]
	v_mul_f32_e32 v191, 0x42800000, v25
	v_mul_f32_e32 v192, 0x42800000, v21
	v_med3_f32 v191, v191, s25, v189
	v_med3_f32 v192, v192, s25, v189
	v_mov_b32_e32 v197, 0
	v_cvt_pk_fp8_f32 v197, v191, v192
	v_mul_f32_e32 v193, 0x42800000, v33
	v_mul_f32_e32 v191, 0x42800000, v29
	v_med3_f32 v192, v193, s25, v189
	v_med3_f32 v191, v191, s25, v189
	v_cvt_pk_fp8_f32 v197, v192, v191 op_sel:[0,0,1]
	s_and_b64 vcc, exec, s[2:3]
	ds_write2_b32 v190, v194, v195 offset0:24 offset1:57
	ds_write2_b32 v190, v196, v197 offset0:90 offset1:123
	s_cbranch_vccnz .LBB0_166
	s_mul_i32 s30, s27, s18
	s_add_i32 s30, s30, s4
	s_lshl_b32 s30, s30, 2
	s_add_u32 s16, s8, s30
	s_addc_u32 s17, s9, 0
	s_lshl_b32 s31, s18, 2
	v_mad_u32_u24 v22, v180, s31, v134
	v_mad_u32_u24 v18, v181, s31, v134
	v_mad_u32_u24 v30, v182, s31, v134
	v_mad_u32_u24 v26, v183, s31, v134
	global_load_dwordx4 v[22:25], v22, s[16:17] nt
	global_load_dwordx4 v[18:21], v18, s[16:17] nt
	global_load_dwordx4 v[30:33], v30, s[16:17] nt
	global_load_dwordx4 v[26:29], v26, s[16:17] nt
.LBB0_166:
	s_waitcnt vmcnt(28)
	v_mul_f32_e32 v191, 0x42800000, v6
	v_mul_f32_e32 v192, 0x42800000, v2
	v_med3_f32 v191, v191, s25, v189
	v_med3_f32 v192, v192, s25, v189
	v_mov_b32_e32 v194, 0
	v_cvt_pk_fp8_f32 v194, v191, v192
	v_mul_f32_e32 v193, 0x42800000, v14
	v_mul_f32_e32 v191, 0x42800000, v10
	v_med3_f32 v192, v193, s25, v189
	v_med3_f32 v191, v191, s25, v189
	v_cvt_pk_fp8_f32 v194, v192, v191 op_sel:[0,0,1]
	v_mul_f32_e32 v191, 0x42800000, v7
	v_mul_f32_e32 v192, 0x42800000, v3
	v_med3_f32 v191, v191, s25, v189
	v_med3_f32 v192, v192, s25, v189
	v_mov_b32_e32 v195, 0
	v_cvt_pk_fp8_f32 v195, v191, v192
	v_mul_f32_e32 v193, 0x42800000, v15
	v_mul_f32_e32 v191, 0x42800000, v11
	v_med3_f32 v192, v193, s25, v189
	v_med3_f32 v191, v191, s25, v189
	v_cvt_pk_fp8_f32 v195, v192, v191 op_sel:[0,0,1]
	v_mul_f32_e32 v191, 0x42800000, v8
	v_mul_f32_e32 v192, 0x42800000, v4
	v_med3_f32 v191, v191, s25, v189
	v_med3_f32 v192, v192, s25, v189
	v_mov_b32_e32 v196, 0
	v_cvt_pk_fp8_f32 v196, v191, v192
	v_mul_f32_e32 v193, 0x42800000, v16
	v_mul_f32_e32 v191, 0x42800000, v12
	v_med3_f32 v192, v193, s25, v189
	v_med3_f32 v191, v191, s25, v189
	v_cvt_pk_fp8_f32 v196, v192, v191 op_sel:[0,0,1]
	v_mul_f32_e32 v191, 0x42800000, v9
	v_mul_f32_e32 v192, 0x42800000, v5
	v_med3_f32 v191, v191, s25, v189
	v_med3_f32 v192, v192, s25, v189
	v_mov_b32_e32 v197, 0
	v_cvt_pk_fp8_f32 v197, v191, v192
	v_mul_f32_e32 v193, 0x42800000, v17
	v_mul_f32_e32 v191, 0x42800000, v13
	v_med3_f32 v192, v193, s25, v189
	v_med3_f32 v191, v191, s25, v189
	v_cvt_pk_fp8_f32 v197, v192, v191 op_sel:[0,0,1]
	s_and_b64 vcc, exec, s[2:3]
	ds_write2_b32 v190, v194, v195 offset0:28 offset1:61
	ds_write2_b32 v190, v196, v197 offset0:94 offset1:127
	s_cbranch_vccnz .LBB0_144
	s_mul_i32 s16, s27, s18
	s_add_i32 s16, s16, s4
	s_lshl_b32 s16, s16, 2
	s_add_u32 s2, s8, s16
	s_addc_u32 s3, s9, 0
	s_lshl_b32 s17, s18, 2
	v_mad_u32_u24 v6, v184, s17, v134
	v_mad_u32_u24 v2, v185, s17, v134
	v_mad_u32_u24 v14, v186, s17, v134
	v_mad_u32_u24 v10, v187, s17, v134
	global_load_dwordx4 v[6:9], v6, s[2:3] nt
	global_load_dwordx4 v[2:5], v2, s[2:3] nt
	global_load_dwordx4 v[14:17], v14, s[2:3] nt
	global_load_dwordx4 v[10:13], v10, s[2:3] nt
	s_branch .LBB0_144

; DI void attn_unit(const Args& A, LAS unsigned char* lds, int unit, int tid, int wave, int lane) {
;     const bf16* Z = (const bf16*)(A.ws + WS_Z); bf16* ao = (bf16*)(A.ws + WS_ATTO); float* al = (float*)(A.ws + WS_ATTL);
;     const int x = unit & 15; int r0 = unit >> 4; const int hh = r0 & 3; r0 >>= 2; const int b = r0 % NB, br = r0 / NB;
;     const int dil = br == 0 ? 1 : (br == 1 ? 4 : 16), lsub = SEQ / dil, nblk = lsub / 128;
;     const int res = x / nblk, nbk = x % nblk, l0 = nbk * 128, wbase = l0 - 64;
;     LAS bf16* Qs = (LAS bf16*)(lds + AT_QS); LAS bf16* Ks = (LAS bf16*)(lds + AT_KS); LAS bf16* Vt = (LAS bf16*)(lds + AT_VT); LAS float* btab = (LAS float*)(lds + AT_BT);
;     __syncthreads();
; #pragma unroll
;     for (int i = 0; i < 2; ++i) { const int id = tid + 512 * i, row = id >> 3, ch = id & 7; const int tok = b * SEQ + (l0 + row) * dil + res;
;         *(LAS u32x4_t*)(Qs + row * AT_QLD + ch * 8) = *(const u32x4_t*)(Z + (size_t)tok * ZLD + ZA + hh * 64 + ch * 8); }
;     for (int id = tid; id < 272 * 8; id += NTHR) { const int row = id >> 3, ch = id & 7; const int pos = wbase + row; u32x4_t v = (u32x4_t){0u, 0u, 0u, 0u};
;         if (row < 256 && pos >= 0 && pos < lsub) v = *(const u32x4_t*)(Z + (size_t)(b * SEQ + pos * dil + res) * ZLD + ZA + 256 + hh * 64 + ch * 8);
;         *(LAS u32x4_t*)(Ks + row * AT_QLD + ch * 8) = v; }
;     for (int id = tid; id < 272 * 8; id += NTHR) { const int key = id % 272, ch = id / 272; const int pos = wbase + key; u32x4_t v = (u32x4_t){0u, 0u, 0u, 0u};
;         if (key < 256 && pos >= 0 && pos < lsub) v = *(const u32x4_t*)(Z + (size_t)(b * SEQ + pos * dil + res) * ZLD + ZA + 512 + hh * 64 + ch * 8);
;         LAS bf16* d = Vt + (ch * 8) * AT_VLD + key;
;         d[0] = (bf16)(v.x & 0xffffu); d[AT_VLD] = (bf16)(v.x >> 16); d[2 * AT_VLD] = (bf16)(v.y & 0xffffu); d[3 * AT_VLD] = (bf16)(v.y >> 16);
;         d[4 * AT_VLD] = (bf16)(v.z & 0xffffu); d[5 * AT_VLD] = (bf16)(v.z >> 16); d[6 * AT_VLD] = (bf16)(v.w & 0xffffu); d[7 * AT_VLD] = (bf16)(v.w >> 16); }
;     if (tid < 129) btab[tid] = A.in[I_RELB][t5_bucket((tid - 64) * dil) * 4 + hh] * 1.4426950408889634f;
;     __syncthreads();
; DI void phase_attn(const Args& A, LAS unsigned char* lds, int u0, int u1, int b0, int nb, int tid, int wave, int lane) {
;     for (int u = u0 + b0; u < u1; u += nb) attn_unit(A, lds, u, tid, wave, lane);
.LBB0_546:
	s_cmp_lt_i32 s6, 5
	s_cselect_b64 s[94:95], -1, 0
	s_and_b64 s[0:1], s[94:95], s[0:1]
	s_andn2_b64 vcc, exec, s[0:1]
	s_cbranch_vccnz .LBB0_957
	s_cmpk_lt_i32 s50, 0xa1
	s_cselect_b64 s[0:1], -1, 0
	s_cmpk_lt_i32 s92, 0xa0
	s_cselect_b64 s[2:3], -1, 0
	s_or_b64 s[0:1], s[2:3], s[0:1]
	s_and_b64 vcc, exec, s[0:1]
	s_cbranch_vccnz .LBB0_640
	s_add_i32 s22, s92, 0xffffff60
	s_cmpk_gt_u32 s22, 0x23f
	s_cbranch_scc1 .LBB0_639
	s_mov_b32 s6, s22
	s_add_i32 s7, s50, 0xffffff60
	s_movk_i32 s8, 0x600
	s_cmpk_lg_i32 s50, 0x100
	s_cbranch_scc1 .Latmap_s22
	s_and_b32 s8, s22, 7
	s_mulk_i32 s8, 0xc0
	s_lshr_b32 s6, s22, 3
	s_add_i32 s6, s6, s8
	s_movk_i32 s7, 12
	s_addk_i32 s8, 0xc0
.Latmap_s22:
	v_readlane_b32 s9, v235, 52
	v_readlane_b32 s2, v235, 9
	v_readlane_b32 s3, v235, 10
	v_readlane_b32 s4, v235, 19
	v_readlane_b32 s5, v235, 20
	s_mov_b32 s72, 0x3e38aa3b
	s_mov_b32 s73, 0x3e38aa3b
	v_lshrrev_b32_e32 v2, 3, v0
	v_and_b32_e32 v3, 7, v0
	v_lshlrev_b32_e32 v3, 4, v3
	s_movk_i32 s39, 0x90
	v_mad_u32_u24 v1, v2, s39, v3
	v_and_b32_e32 v5, 0xff, v0
	v_lshrrev_b32_e32 v6, 8, v0
	s_movk_i32 s39, 0x1180
	v_mul_u32_u24_e32 v4, s39, v6
	v_lshl_add_u32 v4, v5, 1, v4
	v_add_u32_e32 v4, 0xe100, v4
	v_lshlrev_b32_e32 v6, 4, v6
	v_lshlrev_b32_e32 v8, 2, v5
	v_add_u32_e32 v8, 0x16d00, v8
	v_subrev_u32_e32 v165, 16, v0
	s_movk_i32 s39, 0x81
	v_cmp_gt_u32_e64 s[42:43], s39, v165
	s_movk_i32 s39, 0xa0
	v_cmp_gt_u32_e64 s[48:49], s39, v0
	v_cmp_gt_u32_e64 s[46:47], 64, v0
	v_cmp_gt_u32_e64 s[44:45], 16, v146
	v_subrev_u32_e32 v165, 0x50, v0
	v_cmp_lt_i32_e32 vcc, 0, v165
	v_mov_b32_e32 v7, 0
	s_nop 0
	v_cndmask_b32_e64 v166, 0, 16, vcc
	v_lshlrev_b32_e32 v167, 0, v165
	v_sub_u32_e32 v168, 0, v167
	v_max_i32_e32 v167, v167, v168
	v_cvt_f32_u32_e32 v168, v167
	v_mul_f32_e32 v168, 0x3e000000, v168
	v_max_f32_e32 v168, 1.0, v168
	v_log_f32_e32 v168, v168
	v_cmp_gt_u32_e32 vcc, 8, v167
	v_mul_f32_e32 v168, 0x3f924925, v168
	v_cvt_i32_f32_e32 v168, v168
	v_min_i32_e32 v168, 7, v168
	v_add_u32_e32 v168, 8, v168
	v_cndmask_b32_e32 v168, v168, v167, vcc
	v_add_u32_e32 v168, v168, v166
	v_lshl_or_b32 v7, v168, 0, v7
	v_lshlrev_b32_e32 v167, 2, v165
	v_sub_u32_e32 v168, 0, v167
	v_max_i32_e32 v167, v167, v168
	v_cvt_f32_u32_e32 v168, v167
	v_mul_f32_e32 v168, 0x3e000000, v168
	v_max_f32_e32 v168, 1.0, v168
	v_log_f32_e32 v168, v168
	v_cmp_gt_u32_e32 vcc, 8, v167
	v_mul_f32_e32 v168, 0x3f924925, v168
	v_cvt_i32_f32_e32 v168, v168
	v_min_i32_e32 v168, 7, v168
	v_add_u32_e32 v168, 8, v168
	v_cndmask_b32_e32 v168, v168, v167, vcc
	v_add_u32_e32 v168, v168, v166
	v_lshl_or_b32 v7, v168, 8, v7
	v_lshlrev_b32_e32 v167, 4, v165
	v_sub_u32_e32 v168, 0, v167
	v_max_i32_e32 v167, v167, v168
	v_cvt_f32_u32_e32 v168, v167
	v_mul_f32_e32 v168, 0x3e000000, v168
	v_max_f32_e32 v168, 1.0, v168
	v_log_f32_e32 v168, v168
	v_cmp_gt_u32_e32 vcc, 8, v167
	v_mul_f32_e32 v168, 0x3f924925, v168
	v_cvt_i32_f32_e32 v168, v168
	v_min_i32_e32 v168, 7, v168
	v_add_u32_e32 v168, 8, v168
	v_cndmask_b32_e32 v168, v168, v167, vcc
	v_add_u32_e32 v168, v168, v166
	v_lshl_or_b32 v7, v168, 16, v7
	v_and_b32_e32 v165, 15, v146
	v_lshrrev_b32_e32 v166, 4, v146
	s_lshl_b32 s39, s9, 4
	v_add_u32_e32 v40, s39, v165
	s_movk_i32 s40, 0x90
	v_mul_u32_u24_e32 v34, s40, v40
	v_lshl_add_u32 v34, v166, 4, v34
	v_lshlrev_b32_e32 v167, 2, v166
	v_sub_u32_e32 v35, v167, v165
	v_lshlrev_b32_e32 v35, 2, v35
	v_add_u32_e32 v35, 0x16d40, v35
	v_add_u32_e32 v167, s39, v167
	v_lshlrev_b32_e32 v36, 2, v167
	v_add_u32_e32 v36, 0x16f80, v36
	s_movk_i32 s40, 0x230
	v_mul_u32_u24_e32 v37, s40, v165
	v_lshl_add_u32 v37, v167, 1, v37
	v_add_u32_e32 v37, 0xe100, v37
	v_add_u32_e32 v9, 0x2300, v37
	v_add_u32_e32 v118, 0x4600, v37
	v_add_u32_e32 v144, 0x6900, v37
	v_xor_b32_e32 v38, 16, v146
	v_lshlrev_b32_e32 v38, 2, v38
	v_xor_b32_e32 v39, 32, v146
	v_lshlrev_b32_e32 v39, 2, v39
	v_lshlrev_b32_e32 v41, 3, v166
	v_mov_b32_e32 v232, 0
	v_mov_b32_e32 v233, 0
	s_movk_i32 s40, 0x230
	v_mul_u32_u24_e32 v168, s40, v0
	v_add_u32_e32 v168, 0xe300, v168
	s_and_saveexec_b64 s[40:41], s[46:47]
	ds_write_b64 v168, v[232:233] offset:0
	ds_write_b64 v168, v[232:233] offset:8
	ds_write_b64 v168, v[232:233] offset:16
	ds_write_b64 v168, v[232:233] offset:24
	s_mov_b64 exec, s[40:41]
	s_and_b32 s39, s6, 15
	s_bfe_u32 s40, s6, 0x20004
	s_bfe_u32 s41, s6, 0x30006
	s_lshr_b32 s74, s6, 9
	s_lshl_b32 s75, s74, 1
	s_lshl_b32 s16, 1536, s75
	s_add_i32 s20, s75, 9
	s_add_i32 s26, s75, 4
	s_lshl_b32 s28, s74, 3
	s_lshr_b32 s29, 0x800, s75
	s_add_i32 s17, s29, -1
	s_sub_i32 s76, 4, s75
	s_lshr_b32 s77, s39, s76
	s_lshr_b32 s78, 16, s75
	s_add_i32 s78, s78, -1
	s_and_b32 s78, s39, s78
	s_lshl_b32 s19, s78, 7
	s_add_i32 s18, s19, 0xffffffc0
	s_lshl_b32 s79, s41, 11
	s_add_i32 s79, s79, s77
	s_lshl_b32 s80, s40, 7
	s_lshl_b32 s27, s40, 2
	s_mul_i32 s81, s79, 1536
	s_add_u32 s81, s81, s80
	s_add_u32 s81, s81, 0x28600000
	s_add_u32 s10, s2, s81
	s_addc_u32 s11, s3, 0
	s_lshl_b32 s82, s74, 14
	s_add_i32 s82, s82, s79
	s_lshl_b32 s83, s82, 9
	s_add_u32 s83, s83, s80
	s_add_u32 s83, s83, 0x34a00000
	s_add_u32 s12, s2, s83
	s_addc_u32 s13, s3, 0
	s_lshl_b32 s84, s82, 4
	s_add_u32 s84, s84, s27
	s_add_u32 s84, s84, 0x36200000
	s_add_u32 s14, s2, s84
	s_addc_u32 s15, s3, 0
	v_add_u32_e32 v165, s19, v2
	v_mad_u32_u24 v165, v165, s16, v3
	s_lshl_b32 s85, s16, 6
	global_load_dwordx4 v[120:123], v165, s[10:11]
	v_add_u32_e32 v166, s85, v165
	global_load_dwordx4 v[124:127], v166, s[10:11]
	v_add_u32_e32 v167, s18, v2
	v_med3_i32 v168, v167, 0, s17
	v_mad_u32_u24 v168, v168, s16, v3
	global_load_dwordx4 v[128:131], v168, s[10:11] offset:512
	v_add_u32_e32 v168, 64, v167
	v_med3_i32 v168, v168, 0, s17
	v_mad_u32_u24 v168, v168, s16, v3
	global_load_dwordx4 v[132:135], v168, s[10:11] offset:512
	v_add_u32_e32 v168, 0x80, v167
	v_med3_i32 v168, v168, 0, s17
	v_mad_u32_u24 v168, v168, s16, v3
	global_load_dwordx4 v[136:139], v168, s[10:11] offset:512
	v_add_u32_e32 v168, 0xc0, v167
	v_med3_i32 v168, v168, 0, s17
	v_mad_u32_u24 v168, v168, s16, v3
	global_load_dwordx4 v[140:143], v168, s[10:11] offset:512
	v_add_u32_e32 v169, s18, v5
	v_med3_i32 v169, v169, 0, s17
	v_mad_u32_u24 v169, v169, s16, v6
	global_load_dwordx4 v[148:151], v169, s[10:11] offset:1024
	global_load_dwordx4 v[152:155], v169, s[10:11] offset:1056
	global_load_dwordx4 v[156:159], v169, s[10:11] offset:1088
	global_load_dwordx4 v[160:163], v169, s[10:11] offset:1120
	v_bfe_u32 v171, v7, s28, 8
	v_lshl_add_u32 v171, v171, 4, s27
	s_mov_b64 exec, s[42:43]
	global_load_dword v164, v171, s[4:5]
	s_mov_b64 exec, -1

; #define LAS __attribute__((address_space(3)))
; DI unsigned pk4_fp8(float a, float b, float c, float d) { unsigned p = 0u; p = __builtin_amdgcn_cvt_pk_fp8_f32(f8clamp(a), f8clamp(b), p, false); p = __builtin_amdgcn_cvt_pk_fp8_f32(f8clamp(c), f8clamp(d), p, true); return p; }
; DI void f8_convert_reload(f32x4 (&v)[4][4], int hb, float sc, LAS unsigned char* scr, bool reload, const F8Tile& dn, int lane) {
;     const int nq = lane & 15, kq = lane >> 4;
; #pragma unroll
;     for (int it = 0; it < 4; ++it) {
; #pragma unroll
;         for (int i = 0; i < 4; ++i) *(LAS unsigned*)(scr + (4 * nq + i) * 132 + hb * 64 + it * 16 + kq * 4) = pk4_fp8(v[it][0][i] * sc, v[it][1][i] * sc, v[it][2][i] * sc, v[it][3][i] * sc);
;         if (reload) {
; #pragma unroll
;             for (int j = 0; j < 4; ++j) v[it][j] = __builtin_nontemporal_load((const f32x4*)(dn.W + (size_t)(dn.k0 + hb * 64 + it * 16 + kq * 4 + j) * dn.N + dn.n0 + 4 * nq)); } }
; }
.Lcvw2:
	s_waitcnt vmcnt(28)
	v_mul_f32_e32 v134, 0x42800000, v118
	v_mul_f32_e32 v192, 0x42800000, v114
	v_med3_f32 v134, v134, s24, v190
	v_med3_f32 v192, v192, s24, v190
	v_mov_b32_e32 v194, 0
	v_cvt_pk_fp8_f32 v194, v134, v192
	v_mul_f32_e32 v193, 0x42800000, v126
	v_mul_f32_e32 v134, 0x42800000, v122
	v_med3_f32 v192, v193, s24, v190
	v_med3_f32 v134, v134, s24, v190
	v_cvt_pk_fp8_f32 v194, v192, v134 op_sel:[0,0,1]
	v_mul_f32_e32 v134, 0x42800000, v119
	v_mul_f32_e32 v192, 0x42800000, v115
	v_med3_f32 v134, v134, s24, v190
	v_med3_f32 v192, v192, s24, v190
	v_mov_b32_e32 v195, 0
	v_cvt_pk_fp8_f32 v195, v134, v192
	v_mul_f32_e32 v193, 0x42800000, v127
	v_mul_f32_e32 v134, 0x42800000, v123
	v_med3_f32 v192, v193, s24, v190
	v_med3_f32 v134, v134, s24, v190
	v_cvt_pk_fp8_f32 v195, v192, v134 op_sel:[0,0,1]
	v_mul_f32_e32 v134, 0x42800000, v120
	v_mul_f32_e32 v192, 0x42800000, v116
	v_med3_f32 v134, v134, s24, v190
	v_med3_f32 v192, v192, s24, v190
	v_mov_b32_e32 v196, 0
	v_cvt_pk_fp8_f32 v196, v134, v192
	v_mul_f32_e32 v193, 0x42800000, v128
	v_mul_f32_e32 v134, 0x42800000, v124
	v_med3_f32 v192, v193, s24, v190
	v_med3_f32 v134, v134, s24, v190
	v_cvt_pk_fp8_f32 v196, v192, v134 op_sel:[0,0,1]
	v_mul_f32_e32 v134, 0x42800000, v121
	v_mul_f32_e32 v192, 0x42800000, v117
	v_med3_f32 v134, v134, s24, v190
	v_med3_f32 v192, v192, s24, v190
	v_mov_b32_e32 v197, 0
	v_cvt_pk_fp8_f32 v197, v134, v192
	v_mul_f32_e32 v193, 0x42800000, v129
	v_mul_f32_e32 v134, 0x42800000, v125
	v_med3_f32 v192, v193, s24, v190
	v_med3_f32 v134, v134, s24, v190
	v_cvt_pk_fp8_f32 v197, v192, v134 op_sel:[0,0,1]
	v_cndmask_b32_e64 v134, 0, 1, s[14:15]
	v_cmp_ne_u32_e64 s[2:3], 1, v134
	s_andn2_b64 vcc, exec, s[14:15]
	v_lshlrev_b32_e32 v134, 2, v132
	ds_write2_b32 v191, v194, v195 offset1:33
	ds_write2_b32 v191, v196, v197 offset0:66 offset1:99
	s_cbranch_vccnz .LBB0_1356
	s_mul_i32 s28, s26, s16
	s_add_i32 s28, s28, s0
	s_lshl_b32 s28, s28, 2
	s_add_u32 s14, s6, s28
	s_addc_u32 s15, s7, 0
	s_lshl_b32 s29, s16, 2
	v_mad_u32_u24 v118, v1, s29, v134
	v_mad_u32_u24 v114, v133, s29, v134
	v_mad_u32_u24 v126, v158, s29, v134
	v_mad_u32_u24 v122, v159, s29, v134
	global_load_dwordx4 v[118:121], v118, s[14:15] nt
	global_load_dwordx4 v[114:117], v114, s[14:15] nt
	global_load_dwordx4 v[126:129], v126, s[14:15] nt
	global_load_dwordx4 v[122:125], v122, s[14:15] nt
.LBB0_1356:
	s_waitcnt vmcnt(28)
	v_mul_f32_e32 v192, 0x42800000, v102
	v_mul_f32_e32 v193, 0x42800000, v98
	v_med3_f32 v192, v192, s24, v190
	v_med3_f32 v193, v193, s24, v190
	v_mov_b32_e32 v195, 0
	v_cvt_pk_fp8_f32 v195, v192, v193
	v_mul_f32_e32 v194, 0x42800000, v110
	v_mul_f32_e32 v192, 0x42800000, v106
	v_med3_f32 v193, v194, s24, v190
	v_med3_f32 v192, v192, s24, v190
	v_cvt_pk_fp8_f32 v195, v193, v192 op_sel:[0,0,1]
	v_mul_f32_e32 v192, 0x42800000, v103
	v_mul_f32_e32 v193, 0x42800000, v99
	v_med3_f32 v192, v192, s24, v190
	v_med3_f32 v193, v193, s24, v190
	v_mov_b32_e32 v196, 0
	v_cvt_pk_fp8_f32 v196, v192, v193
	v_mul_f32_e32 v194, 0x42800000, v111
	v_mul_f32_e32 v192, 0x42800000, v107
	v_med3_f32 v193, v194, s24, v190
	v_med3_f32 v192, v192, s24, v190
	v_cvt_pk_fp8_f32 v196, v193, v192 op_sel:[0,0,1]
	v_mul_f32_e32 v192, 0x42800000, v104
	v_mul_f32_e32 v193, 0x42800000, v100
	v_med3_f32 v192, v192, s24, v190
	v_med3_f32 v193, v193, s24, v190
	v_mov_b32_e32 v197, 0
	v_cvt_pk_fp8_f32 v197, v192, v193
	v_mul_f32_e32 v194, 0x42800000, v112
	v_mul_f32_e32 v192, 0x42800000, v108
	v_med3_f32 v193, v194, s24, v190
	v_med3_f32 v192, v192, s24, v190
	v_cvt_pk_fp8_f32 v197, v193, v192 op_sel:[0,0,1]
	v_mul_f32_e32 v192, 0x42800000, v105
	v_mul_f32_e32 v193, 0x42800000, v101
	v_med3_f32 v192, v192, s24, v190
	v_med3_f32 v193, v193, s24, v190
	v_mov_b32_e32 v198, 0
	v_cvt_pk_fp8_f32 v198, v192, v193
	v_mul_f32_e32 v194, 0x42800000, v113
	v_mul_f32_e32 v192, 0x42800000, v109
	v_med3_f32 v193, v194, s24, v190
	v_med3_f32 v192, v192, s24, v190
	v_cvt_pk_fp8_f32 v198, v193, v192 op_sel:[0,0,1]
	s_and_b64 vcc, exec, s[2:3]
	ds_write2_b32 v191, v195, v196 offset0:4 offset1:37
	ds_write2_b32 v191, v197, v198 offset0:70 offset1:103
	s_cbranch_vccnz .LBB0_1358
	s_mul_i32 s28, s26, s16
	s_add_i32 s28, s28, s0
	s_lshl_b32 s28, s28, 2
	s_add_u32 s14, s6, s28
	s_addc_u32 s15, s7, 0
	s_lshl_b32 s29, s16, 2
	v_mad_u32_u24 v102, v160, s29, v134
	v_mad_u32_u24 v98, v161, s29, v134
	v_mad_u32_u24 v110, v162, s29, v134
	v_mad_u32_u24 v106, v163, s29, v134
	global_load_dwordx4 v[102:105], v102, s[14:15] nt
	global_load_dwordx4 v[98:101], v98, s[14:15] nt
	global_load_dwordx4 v[110:113], v110, s[14:15] nt
	global_load_dwordx4 v[106:109], v106, s[14:15] nt
; #define LAS __attribute__((address_space(3)))
; DI unsigned pk4_fp8(float a, float b, float c, float d) { unsigned p = 0u; p = __builtin_amdgcn_cvt_pk_fp8_f32(f8clamp(a), f8clamp(b), p, false); p = __builtin_amdgcn_cvt_pk_fp8_f32(f8clamp(c), f8clamp(d), p, true); return p; }
; DI void f8_convert_reload(f32x4 (&v)[4][4], int hb, float sc, LAS unsigned char* scr, bool reload, const F8Tile& dn, int lane) {
;     const int nq = lane & 15, kq = lane >> 4;
; #pragma unroll
;     for (int it = 0; it < 4; ++it) {
; #pragma unroll
;         for (int i = 0; i < 4; ++i) *(LAS unsigned*)(scr + (4 * nq + i) * 132 + hb * 64 + it * 16 + kq * 4) = pk4_fp8(v[it][0][i] * sc, v[it][1][i] * sc, v[it][2][i] * sc, v[it][3][i] * sc);
;         if (reload) {
; #pragma unroll
;             for (int j = 0; j < 4; ++j) v[it][j] = __builtin_nontemporal_load((const f32x4*)(dn.W + (size_t)(dn.k0 + hb * 64 + it * 16 + kq * 4 + j) * dn.N + dn.n0 + 4 * nq)); } }
; }
.LBB0_1358:
	s_waitcnt vmcnt(28)
	v_mul_f32_e32 v192, 0x42800000, v86
	v_mul_f32_e32 v193, 0x42800000, v82
	v_med3_f32 v192, v192, s24, v190
	v_med3_f32 v193, v193, s24, v190
	v_mov_b32_e32 v195, 0
	v_cvt_pk_fp8_f32 v195, v192, v193
	v_mul_f32_e32 v194, 0x42800000, v94
	v_mul_f32_e32 v192, 0x42800000, v90
	v_med3_f32 v193, v194, s24, v190
	v_med3_f32 v192, v192, s24, v190
	v_cvt_pk_fp8_f32 v195, v193, v192 op_sel:[0,0,1]
	v_mul_f32_e32 v192, 0x42800000, v87
	v_mul_f32_e32 v193, 0x42800000, v83
	v_med3_f32 v192, v192, s24, v190
	v_med3_f32 v193, v193, s24, v190
	v_mov_b32_e32 v196, 0
	v_cvt_pk_fp8_f32 v196, v192, v193
	v_mul_f32_e32 v194, 0x42800000, v95
	v_mul_f32_e32 v192, 0x42800000, v91
	v_med3_f32 v193, v194, s24, v190
	v_med3_f32 v192, v192, s24, v190
	v_cvt_pk_fp8_f32 v196, v193, v192 op_sel:[0,0,1]
	v_mul_f32_e32 v192, 0x42800000, v88
	v_mul_f32_e32 v193, 0x42800000, v84
	v_med3_f32 v192, v192, s24, v190
	v_med3_f32 v193, v193, s24, v190
	v_mov_b32_e32 v197, 0
	v_cvt_pk_fp8_f32 v197, v192, v193
	v_mul_f32_e32 v194, 0x42800000, v96
	v_mul_f32_e32 v192, 0x42800000, v92
	v_med3_f32 v193, v194, s24, v190
	v_med3_f32 v192, v192, s24, v190
	v_cvt_pk_fp8_f32 v197, v193, v192 op_sel:[0,0,1]
	v_mul_f32_e32 v192, 0x42800000, v89
	v_mul_f32_e32 v193, 0x42800000, v85
	v_med3_f32 v192, v192, s24, v190
	v_med3_f32 v193, v193, s24, v190
	v_mov_b32_e32 v198, 0
	v_cvt_pk_fp8_f32 v198, v192, v193
	v_mul_f32_e32 v194, 0x42800000, v97
	v_mul_f32_e32 v192, 0x42800000, v93
	v_med3_f32 v193, v194, s24, v190
	v_med3_f32 v192, v192, s24, v190
	v_cvt_pk_fp8_f32 v198, v193, v192 op_sel:[0,0,1]
	s_and_b64 vcc, exec, s[2:3]
	ds_write2_b32 v191, v195, v196 offset0:8 offset1:41
	ds_write2_b32 v191, v197, v198 offset0:74 offset1:107
	s_cbranch_vccnz .LBB0_1360
	s_mul_i32 s28, s26, s16
	s_add_i32 s28, s28, s0
	s_lshl_b32 s28, s28, 2
	s_add_u32 s14, s6, s28
	s_addc_u32 s15, s7, 0
	s_lshl_b32 s29, s16, 2
	v_mad_u32_u24 v86, v164, s29, v134
	v_mad_u32_u24 v82, v165, s29, v134
	v_mad_u32_u24 v94, v166, s29, v134
	v_mad_u32_u24 v90, v167, s29, v134
	global_load_dwordx4 v[86:89], v86, s[14:15] nt
	global_load_dwordx4 v[82:85], v82, s[14:15] nt
	global_load_dwordx4 v[94:97], v94, s[14:15] nt
	global_load_dwordx4 v[90:93], v90, s[14:15] nt
.LBB0_1360:
	s_waitcnt vmcnt(28)
	v_mul_f32_e32 v192, 0x42800000, v70
	v_mul_f32_e32 v193, 0x42800000, v66
	v_med3_f32 v192, v192, s24, v190
	v_med3_f32 v193, v193, s24, v190
	v_mov_b32_e32 v195, 0
	v_cvt_pk_fp8_f32 v195, v192, v193
	v_mul_f32_e32 v194, 0x42800000, v74
	v_mul_f32_e32 v192, 0x42800000, v78
	v_med3_f32 v193, v194, s24, v190
	v_med3_f32 v192, v192, s24, v190
	v_cvt_pk_fp8_f32 v195, v193, v192 op_sel:[0,0,1]
	v_mul_f32_e32 v192, 0x42800000, v71
	v_mul_f32_e32 v193, 0x42800000, v67
	v_med3_f32 v192, v192, s24, v190
	v_med3_f32 v193, v193, s24, v190
	v_mov_b32_e32 v196, 0
	v_cvt_pk_fp8_f32 v196, v192, v193
	v_mul_f32_e32 v194, 0x42800000, v75
	v_mul_f32_e32 v192, 0x42800000, v79
	v_med3_f32 v193, v194, s24, v190
	v_med3_f32 v192, v192, s24, v190
	v_cvt_pk_fp8_f32 v196, v193, v192 op_sel:[0,0,1]
	v_mul_f32_e32 v192, 0x42800000, v72
	v_mul_f32_e32 v193, 0x42800000, v68
	v_med3_f32 v192, v192, s24, v190
	v_med3_f32 v193, v193, s24, v190
	v_mov_b32_e32 v197, 0
	v_cvt_pk_fp8_f32 v197, v192, v193
	v_mul_f32_e32 v194, 0x42800000, v76
	v_mul_f32_e32 v192, 0x42800000, v80
	v_med3_f32 v193, v194, s24, v190
	v_med3_f32 v192, v192, s24, v190
	v_cvt_pk_fp8_f32 v197, v193, v192 op_sel:[0,0,1]
	v_mul_f32_e32 v192, 0x42800000, v73
	v_mul_f32_e32 v193, 0x42800000, v69
	v_med3_f32 v192, v192, s24, v190
	v_med3_f32 v193, v193, s24, v190
	v_mov_b32_e32 v198, 0
	v_cvt_pk_fp8_f32 v198, v192, v193
	v_mul_f32_e32 v194, 0x42800000, v77
	v_mul_f32_e32 v192, 0x42800000, v81
	v_med3_f32 v193, v194, s24, v190
	v_med3_f32 v192, v192, s24, v190
	v_cvt_pk_fp8_f32 v198, v193, v192 op_sel:[0,0,1]
	s_and_b64 vcc, exec, s[2:3]
	ds_write2_b32 v191, v195, v196 offset0:12 offset1:45
	ds_write2_b32 v191, v197, v198 offset0:78 offset1:111
	s_cbranch_vccnz .LBB0_1362
	s_mul_i32 s28, s26, s16
	s_add_i32 s28, s28, s0
	s_lshl_b32 s28, s28, 2
	s_add_u32 s14, s6, s28
	s_addc_u32 s15, s7, 0
	s_lshl_b32 s29, s16, 2
	v_mad_u32_u24 v70, v168, s29, v134
	v_mad_u32_u24 v66, v169, s29, v134
	v_mad_u32_u24 v74, v171, s29, v134
	v_mad_u32_u24 v78, v172, s29, v134
	global_load_dwordx4 v[70:73], v70, s[14:15] nt
	global_load_dwordx4 v[66:69], v66, s[14:15] nt
	global_load_dwordx4 v[74:77], v74, s[14:15] nt
	global_load_dwordx4 v[78:81], v78, s[14:15] nt
.LBB0_1362:
	s_waitcnt vmcnt(28)
	v_mul_f32_e32 v192, 0x42800000, v54
	v_mul_f32_e32 v193, 0x42800000, v50
	v_med3_f32 v192, v192, s24, v190
	v_med3_f32 v193, v193, s24, v190
	v_mov_b32_e32 v195, 0
	v_cvt_pk_fp8_f32 v195, v192, v193
	v_mul_f32_e32 v194, 0x42800000, v62
	v_mul_f32_e32 v192, 0x42800000, v58
	v_med3_f32 v193, v194, s24, v190
	v_med3_f32 v192, v192, s24, v190
	v_cvt_pk_fp8_f32 v195, v193, v192 op_sel:[0,0,1]
	v_mul_f32_e32 v192, 0x42800000, v55
	v_mul_f32_e32 v193, 0x42800000, v51
	v_med3_f32 v192, v192, s24, v190
	v_med3_f32 v193, v193, s24, v190
	v_mov_b32_e32 v196, 0
	v_cvt_pk_fp8_f32 v196, v192, v193
	v_mul_f32_e32 v194, 0x42800000, v63
	v_mul_f32_e32 v192, 0x42800000, v59
	v_med3_f32 v193, v194, s24, v190
	v_med3_f32 v192, v192, s24, v190
	v_cvt_pk_fp8_f32 v196, v193, v192 op_sel:[0,0,1]
	v_mul_f32_e32 v192, 0x42800000, v56
	v_mul_f32_e32 v193, 0x42800000, v52
	v_med3_f32 v192, v192, s24, v190
	v_med3_f32 v193, v193, s24, v190
	v_mov_b32_e32 v197, 0
	v_cvt_pk_fp8_f32 v197, v192, v193
	v_mul_f32_e32 v194, 0x42800000, v64
	v_mul_f32_e32 v192, 0x42800000, v60
	v_med3_f32 v193, v194, s24, v190
	v_med3_f32 v192, v192, s24, v190
	v_cvt_pk_fp8_f32 v197, v193, v192 op_sel:[0,0,1]
	v_mul_f32_e32 v192, 0x42800000, v57
	v_mul_f32_e32 v193, 0x42800000, v53
	v_med3_f32 v192, v192, s24, v190
	v_med3_f32 v193, v193, s24, v190
	v_mov_b32_e32 v198, 0
	v_cvt_pk_fp8_f32 v198, v192, v193
	v_mul_f32_e32 v194, 0x42800000, v65
	v_mul_f32_e32 v192, 0x42800000, v61
	v_med3_f32 v193, v194, s24, v190
	v_med3_f32 v192, v192, s24, v190
	v_cvt_pk_fp8_f32 v198, v193, v192 op_sel:[0,0,1]
	s_and_b64 vcc, exec, s[2:3]
	ds_write2_b32 v191, v195, v196 offset0:16 offset1:49
	ds_write2_b32 v191, v197, v198 offset0:82 offset1:115
	s_cbranch_vccnz .LBB0_1364
	s_mul_i32 s28, s26, s16
	s_add_i32 s28, s28, s0
	s_lshl_b32 s28, s28, 2
	s_add_u32 s14, s6, s28
	s_addc_u32 s15, s7, 0
	s_lshl_b32 s29, s16, 2
	v_mad_u32_u24 v54, v173, s29, v134
	v_mad_u32_u24 v50, v174, s29, v134
	v_mad_u32_u24 v62, v175, s29, v134
	v_mad_u32_u24 v58, v176, s29, v134
	global_load_dwordx4 v[54:57], v54, s[14:15] nt
	global_load_dwordx4 v[50:53], v50, s[14:15] nt
	global_load_dwordx4 v[62:65], v62, s[14:15] nt
	global_load_dwordx4 v[58:61], v58, s[14:15] nt
; #define LAS __attribute__((address_space(3)))
; DI unsigned pk4_fp8(float a, float b, float c, float d) { unsigned p = 0u; p = __builtin_amdgcn_cvt_pk_fp8_f32(f8clamp(a), f8clamp(b), p, false); p = __builtin_amdgcn_cvt_pk_fp8_f32(f8clamp(c), f8clamp(d), p, true); return p; }
; DI void f8_convert_reload(f32x4 (&v)[4][4], int hb, float sc, LAS unsigned char* scr, bool reload, const F8Tile& dn, int lane) {
;     const int nq = lane & 15, kq = lane >> 4;
; #pragma unroll
;     for (int it = 0; it < 4; ++it) {
; #pragma unroll
;         for (int i = 0; i < 4; ++i) *(LAS unsigned*)(scr + (4 * nq + i) * 132 + hb * 64 + it * 16 + kq * 4) = pk4_fp8(v[it][0][i] * sc, v[it][1][i] * sc, v[it][2][i] * sc, v[it][3][i] * sc);
;         if (reload) {
; #pragma unroll
;             for (int j = 0; j < 4; ++j) v[it][j] = __builtin_nontemporal_load((const f32x4*)(dn.W + (size_t)(dn.k0 + hb * 64 + it * 16 + kq * 4 + j) * dn.N + dn.n0 + 4 * nq)); } }
; }
.LBB0_1364:
	s_waitcnt vmcnt(28)
	v_mul_f32_e32 v192, 0x42800000, v38
	v_mul_f32_e32 v193, 0x42800000, v34
	v_med3_f32 v192, v192, s24, v190
	v_med3_f32 v193, v193, s24, v190
	v_mov_b32_e32 v195, 0
	v_cvt_pk_fp8_f32 v195, v192, v193
	v_mul_f32_e32 v194, 0x42800000, v46
	v_mul_f32_e32 v192, 0x42800000, v42
	v_med3_f32 v193, v194, s24, v190
	v_med3_f32 v192, v192, s24, v190
	v_cvt_pk_fp8_f32 v195, v193, v192 op_sel:[0,0,1]
	v_mul_f32_e32 v192, 0x42800000, v39
	v_mul_f32_e32 v193, 0x42800000, v35
	v_med3_f32 v192, v192, s24, v190
	v_med3_f32 v193, v193, s24, v190
	v_mov_b32_e32 v196, 0
	v_cvt_pk_fp8_f32 v196, v192, v193
	v_mul_f32_e32 v194, 0x42800000, v47
	v_mul_f32_e32 v192, 0x42800000, v43
	v_med3_f32 v193, v194, s24, v190
	v_med3_f32 v192, v192, s24, v190
	v_cvt_pk_fp8_f32 v196, v193, v192 op_sel:[0,0,1]
	v_mul_f32_e32 v192, 0x42800000, v40
	v_mul_f32_e32 v193, 0x42800000, v36
	v_med3_f32 v192, v192, s24, v190
	v_med3_f32 v193, v193, s24, v190
	v_mov_b32_e32 v197, 0
	v_cvt_pk_fp8_f32 v197, v192, v193
	v_mul_f32_e32 v194, 0x42800000, v48
	v_mul_f32_e32 v192, 0x42800000, v44
	v_med3_f32 v193, v194, s24, v190
	v_med3_f32 v192, v192, s24, v190
	v_cvt_pk_fp8_f32 v197, v193, v192 op_sel:[0,0,1]
	v_mul_f32_e32 v192, 0x42800000, v41
	v_mul_f32_e32 v193, 0x42800000, v37
	v_med3_f32 v192, v192, s24, v190
	v_med3_f32 v193, v193, s24, v190
	v_mov_b32_e32 v198, 0
	v_cvt_pk_fp8_f32 v198, v192, v193
	v_mul_f32_e32 v194, 0x42800000, v49
	v_mul_f32_e32 v192, 0x42800000, v45
	v_med3_f32 v193, v194, s24, v190
	v_med3_f32 v192, v192, s24, v190
	v_cvt_pk_fp8_f32 v198, v193, v192 op_sel:[0,0,1]
	s_and_b64 vcc, exec, s[2:3]
	ds_write2_b32 v191, v195, v196 offset0:20 offset1:53
	ds_write2_b32 v191, v197, v198 offset0:86 offset1:119
	s_cbranch_vccnz .LBB0_1366
	s_mul_i32 s28, s26, s16
	s_add_i32 s28, s28, s0
	s_lshl_b32 s28, s28, 2
	s_add_u32 s14, s6, s28
	s_addc_u32 s15, s7, 0
	s_lshl_b32 s29, s16, 2
	v_mad_u32_u24 v38, v177, s29, v134
	v_mad_u32_u24 v34, v178, s29, v134
	v_mad_u32_u24 v46, v179, s29, v134
	v_mad_u32_u24 v42, v180, s29, v134
	global_load_dwordx4 v[38:41], v38, s[14:15] nt
	global_load_dwordx4 v[34:37], v34, s[14:15] nt
	global_load_dwordx4 v[46:49], v46, s[14:15] nt
	global_load_dwordx4 v[42:45], v42, s[14:15] nt
.LBB0_1366:
	s_waitcnt vmcnt(28)
	v_mul_f32_e32 v192, 0x42800000, v22
	v_mul_f32_e32 v193, 0x42800000, v18
	v_med3_f32 v192, v192, s24, v190
	v_med3_f32 v193, v193, s24, v190
	v_mov_b32_e32 v195, 0
	v_cvt_pk_fp8_f32 v195, v192, v193
	v_mul_f32_e32 v194, 0x42800000, v30
	v_mul_f32_e32 v192, 0x42800000, v26
	v_med3_f32 v193, v194, s24, v190
	v_med3_f32 v192, v192, s24, v190
	v_cvt_pk_fp8_f32 v195, v193, v192 op_sel:[0,0,1]
	v_mul_f32_e32 v192, 0x42800000, v23
	v_mul_f32_e32 v193, 0x42800000, v19
	v_med3_f32 v192, v192, s24, v190
	v_med3_f32 v193, v193, s24, v190
	v_mov_b32_e32 v196, 0
	v_cvt_pk_fp8_f32 v196, v192, v193
	v_mul_f32_e32 v194, 0x42800000, v31
	v_mul_f32_e32 v192, 0x42800000, v27
	v_med3_f32 v193, v194, s24, v190
	v_med3_f32 v192, v192, s24, v190
	v_cvt_pk_fp8_f32 v196, v193, v192 op_sel:[0,0,1]
	v_mul_f32_e32 v192, 0x42800000, v24
	v_mul_f32_e32 v193, 0x42800000, v20
	v_med3_f32 v192, v192, s24, v190
	v_med3_f32 v193, v193, s24, v190
	v_mov_b32_e32 v197, 0
	v_cvt_pk_fp8_f32 v197, v192, v193
	v_mul_f32_e32 v194, 0x42800000, v32
	v_mul_f32_e32 v192, 0x42800000, v28
	v_med3_f32 v193, v194, s24, v190
	v_med3_f32 v192, v192, s24, v190
	v_cvt_pk_fp8_f32 v197, v193, v192 op_sel:[0,0,1]
	v_mul_f32_e32 v192, 0x42800000, v25
	v_mul_f32_e32 v193, 0x42800000, v21
	v_med3_f32 v192, v192, s24, v190
	v_med3_f32 v193, v193, s24, v190
	v_mov_b32_e32 v198, 0
	v_cvt_pk_fp8_f32 v198, v192, v193
	v_mul_f32_e32 v194, 0x42800000, v33
	v_mul_f32_e32 v192, 0x42800000, v29
	v_med3_f32 v193, v194, s24, v190
	v_med3_f32 v192, v192, s24, v190
	v_cvt_pk_fp8_f32 v198, v193, v192 op_sel:[0,0,1]
	s_and_b64 vcc, exec, s[2:3]
	ds_write2_b32 v191, v195, v196 offset0:24 offset1:57
	ds_write2_b32 v191, v197, v198 offset0:90 offset1:123
	s_cbranch_vccnz .LBB0_1368
	s_mul_i32 s28, s26, s16
	s_add_i32 s28, s28, s0
	s_lshl_b32 s28, s28, 2
	s_add_u32 s14, s6, s28
	s_addc_u32 s15, s7, 0
	s_lshl_b32 s29, s16, 2
	v_mad_u32_u24 v22, v181, s29, v134
	v_mad_u32_u24 v18, v182, s29, v134
	v_mad_u32_u24 v30, v183, s29, v134
	v_mad_u32_u24 v26, v184, s29, v134
	global_load_dwordx4 v[22:25], v22, s[14:15] nt
	global_load_dwordx4 v[18:21], v18, s[14:15] nt
	global_load_dwordx4 v[30:33], v30, s[14:15] nt
	global_load_dwordx4 v[26:29], v26, s[14:15] nt
.LBB0_1368:
	s_waitcnt vmcnt(28)
	v_mul_f32_e32 v192, 0x42800000, v6
	v_mul_f32_e32 v193, 0x42800000, v2
	v_med3_f32 v192, v192, s24, v190
	v_med3_f32 v193, v193, s24, v190
	v_mov_b32_e32 v195, 0
	v_cvt_pk_fp8_f32 v195, v192, v193
	v_mul_f32_e32 v194, 0x42800000, v14
	v_mul_f32_e32 v192, 0x42800000, v10
	v_med3_f32 v193, v194, s24, v190
	v_med3_f32 v192, v192, s24, v190
	v_cvt_pk_fp8_f32 v195, v193, v192 op_sel:[0,0,1]
	v_mul_f32_e32 v192, 0x42800000, v7
	v_mul_f32_e32 v193, 0x42800000, v3
	v_med3_f32 v192, v192, s24, v190
	v_med3_f32 v193, v193, s24, v190
	v_mov_b32_e32 v196, 0
	v_cvt_pk_fp8_f32 v196, v192, v193
	v_mul_f32_e32 v194, 0x42800000, v15
	v_mul_f32_e32 v192, 0x42800000, v11
	v_med3_f32 v193, v194, s24, v190
	v_med3_f32 v192, v192, s24, v190
	v_cvt_pk_fp8_f32 v196, v193, v192 op_sel:[0,0,1]
	v_mul_f32_e32 v192, 0x42800000, v8
	v_mul_f32_e32 v193, 0x42800000, v4
	v_med3_f32 v192, v192, s24, v190
	v_med3_f32 v193, v193, s24, v190
	v_mov_b32_e32 v197, 0
	v_cvt_pk_fp8_f32 v197, v192, v193
	v_mul_f32_e32 v194, 0x42800000, v16
	v_mul_f32_e32 v192, 0x42800000, v12
	v_med3_f32 v193, v194, s24, v190
	v_med3_f32 v192, v192, s24, v190
	v_cvt_pk_fp8_f32 v197, v193, v192 op_sel:[0,0,1]
	v_mul_f32_e32 v192, 0x42800000, v9
	v_mul_f32_e32 v193, 0x42800000, v5
	v_med3_f32 v192, v192, s24, v190
	v_med3_f32 v193, v193, s24, v190
	v_mov_b32_e32 v198, 0
	v_cvt_pk_fp8_f32 v198, v192, v193
	v_mul_f32_e32 v194, 0x42800000, v17
	v_mul_f32_e32 v192, 0x42800000, v13
	v_med3_f32 v193, v194, s24, v190
	v_med3_f32 v192, v192, s24, v190
	v_cvt_pk_fp8_f32 v198, v193, v192 op_sel:[0,0,1]
	s_and_b64 vcc, exec, s[2:3]
	ds_write2_b32 v191, v195, v196 offset0:28 offset1:61
	ds_write2_b32 v191, v197, v198 offset0:94 offset1:127
	s_cbranch_vccnz .LBB0_1346
	s_mul_i32 s14, s26, s16
	s_add_i32 s14, s14, s0
	s_lshl_b32 s14, s14, 2
	s_add_u32 s2, s6, s14
	s_addc_u32 s3, s7, 0
	s_lshl_b32 s15, s16, 2
	v_mad_u32_u24 v6, v185, s15, v134
	v_mad_u32_u24 v2, v186, s15, v134
	v_mad_u32_u24 v14, v187, s15, v134
	v_mad_u32_u24 v10, v188, s15, v134
	global_load_dwordx4 v[6:9], v6, s[2:3] nt
	global_load_dwordx4 v[2:5], v2, s[2:3] nt
	global_load_dwordx4 v[14:17], v14, s[2:3] nt
	global_load_dwordx4 v[10:13], v10, s[2:3] nt
	s_branch .LBB0_1346

; #define LAS __attribute__((address_space(3)))
; DI void phase_attn(const Args& A, LAS unsigned char* lds, int u0, int u1, int b0, int nb, int tid, int wave, int lane) {
;     for (int u = u0 + b0; u < u1; u += nb) attn_unit(A, lds, u, tid, wave, lane);
; template <int l> DI void run_layer(const Args& A, LAS unsigned char* lds, const XcdBarrier& bar, int lo, int hi, int G, int bid, int tid, int lane, int wave, int gw, int ngw, int gtid, int nthr) {
;     ...
;           if (G > ATT_SCAN_BLK0 && bid >= ATT_SCAN_BLK0) phase_attn(A, lds, 0, ATT_UNITS - ATT_SPLIT, bid - ATT_SCAN_BLK0, G - ATT_SCAN_BLK0, tid, wave, lane);
.LBB0_2008:
	s_cmp_lt_i32 s6, 15
	s_cselect_b64 s[24:25], -1, 0
	s_and_b64 s[0:1], s[24:25], s[0:1]
	s_andn2_b64 vcc, exec, s[0:1]
	s_cbranch_vccnz .LBB0_2420
	s_cmpk_lt_i32 s50, 0xa1
	s_cselect_b64 s[0:1], -1, 0
	s_cmpk_lt_i32 s92, 0xa0
	s_cselect_b64 s[2:3], -1, 0
	s_or_b64 s[0:1], s[2:3], s[0:1]
	s_and_b64 vcc, exec, s[0:1]
	s_cbranch_vccnz .LBB0_2102
	s_add_i32 s33, s92, 0xffffff60
	s_cmpk_gt_u32 s33, 0x23f
	s_cbranch_scc1 .LBB0_2101
	s_mov_b32 s6, s33
	s_add_i32 s7, s50, 0xffffff60
	s_movk_i32 s8, 0x600
	s_cmpk_lg_i32 s50, 0x100
	s_cbranch_scc1 .Latmap_s33
	s_and_b32 s8, s33, 7
	s_mulk_i32 s8, 0xc0
	s_lshr_b32 s6, s33, 3
	s_add_i32 s6, s6, s8
	s_movk_i32 s7, 12
	s_addk_i32 s8, 0xc0
